# MoE weight conversion rewritten by hand (lane = column, full-line stores) and moved into layer 0's differential-attention phase: half of the workgroups convert before their attention units, the other
# speedup vs baseline: 1.0148x; 1.0148x over previous
.LBB0_37:
.LBB0_55:
	s_waitcnt vmcnt(13)
	v_lshl_add_u32 v18, s2, 9, v69
	s_mov_b32 s1, 0x180000
	v_cmp_gt_i32_e32 vcc, s1, v18
	s_and_saveexec_b64 s[10:11], vcc
	s_cbranch_execz .LBB0_66
	s_waitcnt lgkmcnt(0)
	s_mov_b64 s[4:5], 0x3a400000
	v_lshl_add_u64 v[0:1], v[70:71], 0, s[4:5]
	s_mov_b64 s[4:5], 0x3a600000
	v_lshl_add_u64 v[2:3], v[70:71], 0, s[4:5]
	s_mov_b64 s[4:5], 0x3a800000
	v_lshl_add_u64 v[4:5], v[70:71], 0, s[4:5]
	s_mov_b64 s[4:5], 0x3ac00000
	s_mov_b32 s14, 0x6dc9c883
	v_lshl_add_u64 v[6:7], v[70:71], 0, s[4:5]
	s_lshl_b32 s1, s33, 9
	s_mov_b64 s[12:13], 0
	s_mov_b32 s3, 0x2aaaaaab
	s_movk_i32 s9, 0x60
	s_mov_b32 s15, 0x3fc45f30
	v_mov_b32_e32 v9, 0
	s_mov_b32 s18, 0x17ffff
	s_waitcnt vmcnt(12)
	v_mov_b32_e32 v19, 0x3febb5fa
	s_waitcnt vmcnt(11)
	v_mov_b32_e32 v20, 0x3fe7ff22
	s_waitcnt vmcnt(10)
	v_mov_b32_e32 v21, 0xd00ab22c
	s_waitcnt vmcnt(9)
	v_mov_b32_e32 v22, 0x24115d9a
	s_branch .LBB0_58

.LBB0_370:
	s_or_b64 exec, exec, s[4:5]
	v_readlane_b32 s14, v255, 29
	s_waitcnt lgkmcnt(0)
	s_barrier
	v_readlane_b32 s0, v255, 29
	v_readlane_b32 s3, v255, 5
	s_nop 4
	s_cmp_lg_u32 s0, s3
	s_cbranch_scc1 .Lcv_ret0
	s_bitcmp1_b32 s2, 3
	s_cbranch_scc0 .Lcv_ret0
	s_mov_b32 s53, 0
	s_branch .Lcv_body
.Lcv_ret0:
	s_mov_b32 s12, 0
	v_mbcnt_lo_u32_b32 v1, -1, 0
	v_mbcnt_hi_u32_b32 v1, -1, v1
	v_readlane_b32 s15, v255, 30
	v_add_u32_e32 v176, s95, v1
	s_load_dwordx8 s[4:11], s[14:15], 0x18
	s_load_dwordx4 s[16:19], s[14:15], 0x38
	v_and_b32_e32 v175, 63, v176
	v_lshlrev_b32_e32 v2, 2, v175
	s_waitcnt lgkmcnt(0)
	global_load_dword v1, v2, s[8:9]
	global_load_dword v4, v2, s[10:11]
	global_load_dword v6, v2, s[16:17]
	global_load_dword v7, v2, s[18:19]
	v_xor_b32_e32 v172, 4, v2
	v_xor_b32_e32 v173, 8, v2
	v_xor_b32_e32 v174, 16, v2
	v_cndmask_b32_e64 v0, v218, v202, s[76:77]
	s_mov_b32 s13, s45
	s_waitcnt vmcnt(2)
	v_mul_f32_e32 v5, v1, v4
	s_waitcnt vmcnt(0)
	v_mul_f32_e32 v8, v6, v7
	ds_bpermute_b32 v5, v172, v5
	ds_bpermute_b32 v8, v172, v8
	s_waitcnt lgkmcnt(1)
	v_fmac_f32_e32 v5, v1, v4
	s_waitcnt lgkmcnt(0)
	v_fmac_f32_e32 v8, v6, v7
	ds_bpermute_b32 v1, v173, v5
	ds_bpermute_b32 v6, v173, v8
	s_waitcnt lgkmcnt(1)
	v_add_f32_e32 v1, v5, v1
	s_waitcnt lgkmcnt(0)
	v_add_f32_e32 v6, v8, v6
	ds_bpermute_b32 v4, v174, v1
	ds_bpermute_b32 v7, v174, v6
	s_waitcnt lgkmcnt(1)
	v_add_f32_e32 v1, v1, v4
	v_xor_b32_e32 v4, 32, v2
	s_waitcnt lgkmcnt(0)
	v_add_f32_e32 v6, v6, v7
	ds_bpermute_b32 v5, v4, v1
	ds_bpermute_b32 v7, v4, v6
	s_waitcnt lgkmcnt(1)
	v_add_f32_e32 v1, v1, v5
	v_xor_b32_e32 v5, 64, v2
	s_waitcnt lgkmcnt(0)
	v_add_f32_e32 v6, v6, v7
	ds_bpermute_b32 v9, v5, v1
	ds_bpermute_b32 v7, v5, v6
	s_waitcnt lgkmcnt(1)
	v_add_f32_e32 v9, v1, v9
	v_xor_b32_e32 v1, 0x80, v2
	s_waitcnt lgkmcnt(0)
	v_add_f32_e32 v6, v6, v7
	ds_bpermute_b32 v10, v1, v9
	ds_bpermute_b32 v7, v1, v6
	s_waitcnt lgkmcnt(1)
	v_add_f32_e32 v9, v9, v10
	s_waitcnt lgkmcnt(0)
	v_add_f32_e32 v6, v6, v7
	v_mul_f32_e32 v7, 0x3fb8aa3b, v9
	v_mul_f32_e32 v6, 0x3fb8aa3b, v6
	v_exp_f32_e32 v7, v7
	v_exp_f32_e32 v6, v6
	s_nop 0
	v_sub_f32_e32 v6, v7, v6
	v_add_f32_e32 v6, v0, v6
	s_nop 0
	v_readfirstlane_b32 s14, v6
	global_load_dword v6, v2, s[4:5]
	v_readlane_b32 s4, v253, 14
	global_load_dword v2, v2, s[6:7]
	v_readlane_b32 s5, v253, 15
	s_andn2_b64 vcc, exec, s[4:5]
	s_waitcnt vmcnt(1)
	v_max_f32_e64 v6, |v6|, |v6|
	v_max_f32_e32 v6, 0, v6
	ds_bpermute_b32 v7, v172, v6
	s_waitcnt vmcnt(0)
	v_max_f32_e64 v2, |v2|, |v2|
	v_max_f32_e32 v2, 0, v2
	s_waitcnt lgkmcnt(0)
	v_max_f32_e32 v7, v7, v7
	v_max_f32_e32 v6, v6, v7
	ds_bpermute_b32 v7, v173, v6
	s_waitcnt lgkmcnt(0)
	v_max_f32_e32 v7, v7, v7
	v_max_f32_e32 v6, v6, v7
	ds_bpermute_b32 v7, v174, v6
	s_waitcnt lgkmcnt(0)
	v_max_f32_e32 v7, v7, v7
	v_max_f32_e32 v6, v6, v7
	ds_bpermute_b32 v7, v4, v6
	s_waitcnt lgkmcnt(0)
	v_max_f32_e32 v7, v7, v7
	v_max_f32_e32 v6, v6, v7
	ds_bpermute_b32 v7, v5, v6
	s_waitcnt lgkmcnt(0)
	v_max_f32_e32 v7, v7, v7
	v_max_f32_e32 v6, v6, v7
	ds_bpermute_b32 v7, v1, v6
	s_waitcnt lgkmcnt(0)
	v_max_f32_e32 v7, v7, v7
	v_max_f32_e32 v6, v6, v7
	ds_bpermute_b32 v7, v172, v2
	v_mul_f32_e32 v6, 0x413c5bb7, v6
	s_waitcnt lgkmcnt(0)
	v_max_f32_e32 v7, v7, v7
	v_max_f32_e32 v2, v2, v7
	ds_bpermute_b32 v7, v173, v2
	s_waitcnt lgkmcnt(0)
	v_max_f32_e32 v7, v7, v7
	v_max_f32_e32 v2, v2, v7
	ds_bpermute_b32 v7, v174, v2
	s_waitcnt lgkmcnt(0)
	v_max_f32_e32 v7, v7, v7
	v_max_f32_e32 v2, v2, v7
	ds_bpermute_b32 v4, v4, v2
	s_waitcnt lgkmcnt(0)
	v_max_f32_e32 v4, v4, v4
	v_max_f32_e32 v2, v2, v4
	ds_bpermute_b32 v4, v5, v2
	s_waitcnt lgkmcnt(0)
	v_max_f32_e32 v4, v4, v4
	v_max_f32_e32 v2, v2, v4
	ds_bpermute_b32 v1, v1, v2
	s_waitcnt lgkmcnt(0)
	v_max_f32_e32 v1, v1, v1
	v_max_f32_e32 v1, v2, v1
	v_mul_f32_e32 v1, v6, v1
	s_nop 0
	v_readfirstlane_b32 s0, v1
	s_cbranch_vccnz .LBB0_380
	v_readlane_b32 s4, v254, 42
	v_readlane_b32 s6, v254, 44
	v_readlane_b32 s5, v254, 43
	v_readlane_b32 s7, v254, 45
	s_add_u32 s4, s6, s12
	s_addc_u32 s5, s7, 0
	v_readlane_b32 s6, v255, 29
	v_sub_f32_e32 v177, 1.0, v0
	v_mov_b32_e32 v0, s0
	v_readlane_b32 s7, v255, 30
	s_add_u32 s0, s4, 0x4c200000
	s_load_dwordx2 s[8:9], s[6:7], 0x48
	s_addc_u32 s3, s5, 0
	s_add_u32 s15, s4, 0x40200000
	s_addc_u32 s16, s5, 0
	v_sub_f32_e32 v36, 0x410ccccd, v0
	s_add_u32 s17, s4, 0x36400000
	v_mov_b32_e32 v37, v36
	v_mov_b32_e32 v38, v36
	v_mov_b32_e32 v39, v36
	s_addc_u32 s18, s5, 0
	s_mov_b32 s19, s2
	s_branch .LBB0_373

.LBB0_383:
	v_readlane_b32 s0, v255, 29
	v_readlane_b32 s3, v255, 5
	s_nop 4
	s_cmp_lg_u32 s0, s3
	s_cbranch_scc1 .Lcv_ret1
	s_bitcmp1_b32 s2, 3
	s_cbranch_scc1 .Lcv_ret1
	s_mov_b32 s53, 1
	s_branch .Lcv_body

.Lcv_body:
	v_readlane_b32 s40, v255, 5
	v_readlane_b32 s41, v255, 6
	v_mbcnt_lo_u32_b32 v0, -1, 0
	v_mbcnt_hi_u32_b32 v0, -1, v0
	s_nop 4
	s_load_dwordx2 s[34:35], s[40:41], 0x128
	v_lshlrev_b32_e32 v1, 2, v0
	s_mov_b32 s31, 0x7fffff
	s_lshr_b32 s47, s95, 6
	s_lshl_b32 s3, s2, 3
	s_add_i32 s47, s47, s3
	s_mov_b32 s0, 0
	s_waitcnt lgkmcnt(0)
.Lcv_unit:
	s_cmp_lt_u32 s0, 14
	s_cbranch_scc0 .Lcv_fp8
	s_cmp_ge_u32 s0, 7
	s_cselect_b32 s32, 1, 0
	s_mul_i32 s3, s32, 7
	s_sub_i32 s3, s0, s3
	s_lshl_b32 s3, s3, 11
	s_add_i32 s3, s3, s47
	s_lshr_b32 s16, s3, 8
	s_mul_i32 s16, s16, 37
	s_lshr_b32 s16, s16, 8
	s_mul_i32 s44, s16, 0x700
	s_sub_i32 s3, s3, s44
	s_lshr_b32 s44, s3, 4
	s_mulk_i32 s44, 0x93
	s_lshr_b32 s44, s44, 10
	s_mul_i32 s12, s44, 0x70
	s_sub_i32 s3, s3, s12
	s_lshl_b32 s12, s32, 3
	s_add_i32 s12, s12, 0x108
	s_load_dwordx2 s[6:7], s[40:41], s12
	s_mul_i32 s12, s16, 0x3800000
	s_mul_i32 s13, s44, 0x380000
	s_add_u32 s12, s12, s13
	s_lshl_b32 s13, s3, 8
	s_add_u32 s12, s12, s13
	s_mov_b32 s15, 0x7000
	s_waitcnt lgkmcnt(0)
	s_add_u32 s4, s6, s12
	s_addc_u32 s5, s7, 0
	s_mul_i32 s12, s16, 0x1c00000
	s_lshl_b32 s13, s44, 7
	s_add_u32 s12, s12, s13
	s_add_u32 s12, s12, 0x8400000
	s_add_u32 s8, s34, s12
	s_addc_u32 s9, s35, 0
	v_lshl_add_u32 v5, s3, 6, v0
	v_lshrrev_b32_e32 v70, 7, v5
	v_and_b32_e32 v132, 0x7f, v5
	v_lshl_add_u32 v70, v70, 8, v132
	s_lshl_b32 s13, s32, 7
	v_add_u32_e32 v70, s13, v70
	v_lshlrev_b32_e32 v2, 11, v70
	global_load_dword v20, v1, s[4:5] nt
	s_add_u32 s4, s4, s15
	s_addc_u32 s5, s5, 0
	global_load_dword v21, v1, s[4:5] nt
	s_add_u32 s4, s4, s15
	s_addc_u32 s5, s5, 0
	global_load_dword v22, v1, s[4:5] nt
	s_add_u32 s4, s4, s15
	s_addc_u32 s5, s5, 0
	global_load_dword v23, v1, s[4:5] nt
	s_add_u32 s4, s4, s15
	s_addc_u32 s5, s5, 0
	global_load_dword v24, v1, s[4:5] nt
	s_add_u32 s4, s4, s15
	s_addc_u32 s5, s5, 0
	global_load_dword v25, v1, s[4:5] nt
	s_add_u32 s4, s4, s15
	s_addc_u32 s5, s5, 0
	global_load_dword v26, v1, s[4:5] nt
	s_add_u32 s4, s4, s15
	s_addc_u32 s5, s5, 0
	global_load_dword v27, v1, s[4:5] nt
	s_add_u32 s4, s4, s15
	s_addc_u32 s5, s5, 0
	global_load_dword v28, v1, s[4:5] nt
	s_add_u32 s4, s4, s15
	s_addc_u32 s5, s5, 0
	global_load_dword v29, v1, s[4:5] nt
	s_add_u32 s4, s4, s15
	s_addc_u32 s5, s5, 0
	global_load_dword v30, v1, s[4:5] nt
	s_add_u32 s4, s4, s15
	s_addc_u32 s5, s5, 0
	global_load_dword v31, v1, s[4:5] nt
	s_add_u32 s4, s4, s15
	s_addc_u32 s5, s5, 0
	global_load_dword v32, v1, s[4:5] nt
	s_add_u32 s4, s4, s15
	s_addc_u32 s5, s5, 0
	global_load_dword v33, v1, s[4:5] nt
	s_add_u32 s4, s4, s15
	s_addc_u32 s5, s5, 0
	global_load_dword v34, v1, s[4:5] nt
	s_add_u32 s4, s4, s15
	s_addc_u32 s5, s5, 0
	global_load_dword v35, v1, s[4:5] nt
	s_add_u32 s4, s4, s15
	s_addc_u32 s5, s5, 0
	global_load_dword v36, v1, s[4:5] nt
	s_add_u32 s4, s4, s15
	s_addc_u32 s5, s5, 0
	global_load_dword v37, v1, s[4:5] nt
	s_add_u32 s4, s4, s15
	s_addc_u32 s5, s5, 0
	global_load_dword v38, v1, s[4:5] nt
	s_add_u32 s4, s4, s15
	s_addc_u32 s5, s5, 0
	global_load_dword v39, v1, s[4:5] nt
	s_add_u32 s4, s4, s15
	s_addc_u32 s5, s5, 0
	global_load_dword v40, v1, s[4:5] nt
	s_add_u32 s4, s4, s15
	s_addc_u32 s5, s5, 0
	global_load_dword v41, v1, s[4:5] nt
	s_add_u32 s4, s4, s15
	s_addc_u32 s5, s5, 0
	global_load_dword v42, v1, s[4:5] nt
	s_add_u32 s4, s4, s15
	s_addc_u32 s5, s5, 0
	global_load_dword v43, v1, s[4:5] nt
	s_add_u32 s4, s4, s15
	s_addc_u32 s5, s5, 0
	global_load_dword v44, v1, s[4:5] nt
	s_add_u32 s4, s4, s15
	s_addc_u32 s5, s5, 0
	global_load_dword v45, v1, s[4:5] nt
	s_add_u32 s4, s4, s15
	s_addc_u32 s5, s5, 0
	global_load_dword v46, v1, s[4:5] nt
	s_add_u32 s4, s4, s15
	s_addc_u32 s5, s5, 0
	global_load_dword v47, v1, s[4:5] nt
	s_add_u32 s4, s4, s15
	s_addc_u32 s5, s5, 0
	global_load_dword v48, v1, s[4:5] nt
	s_add_u32 s4, s4, s15
	s_addc_u32 s5, s5, 0
	global_load_dword v49, v1, s[4:5] nt
	s_add_u32 s4, s4, s15
	s_addc_u32 s5, s5, 0
	global_load_dword v50, v1, s[4:5] nt
	s_add_u32 s4, s4, s15
	s_addc_u32 s5, s5, 0
	global_load_dword v51, v1, s[4:5] nt
	s_add_u32 s4, s4, s15
	s_addc_u32 s5, s5, 0
	global_load_dword v148, v1, s[4:5] nt
	s_add_u32 s4, s4, s15
	s_addc_u32 s5, s5, 0
	global_load_dword v149, v1, s[4:5] nt
	s_add_u32 s4, s4, s15
	s_addc_u32 s5, s5, 0
	global_load_dword v150, v1, s[4:5] nt
	s_add_u32 s4, s4, s15
	s_addc_u32 s5, s5, 0
	global_load_dword v151, v1, s[4:5] nt
	s_add_u32 s4, s4, s15
	s_addc_u32 s5, s5, 0
	global_load_dword v152, v1, s[4:5] nt
	s_add_u32 s4, s4, s15
	s_addc_u32 s5, s5, 0
	global_load_dword v153, v1, s[4:5] nt
	s_add_u32 s4, s4, s15
	s_addc_u32 s5, s5, 0
	global_load_dword v154, v1, s[4:5] nt
	s_add_u32 s4, s4, s15
	s_addc_u32 s5, s5, 0
	global_load_dword v155, v1, s[4:5] nt
	s_add_u32 s4, s4, s15
	s_addc_u32 s5, s5, 0
	global_load_dword v156, v1, s[4:5] nt
	s_add_u32 s4, s4, s15
	s_addc_u32 s5, s5, 0
	global_load_dword v157, v1, s[4:5] nt
	s_add_u32 s4, s4, s15
	s_addc_u32 s5, s5, 0
	global_load_dword v158, v1, s[4:5] nt
	s_add_u32 s4, s4, s15
	s_addc_u32 s5, s5, 0
	global_load_dword v159, v1, s[4:5] nt
	s_add_u32 s4, s4, s15
	s_addc_u32 s5, s5, 0
	global_load_dword v160, v1, s[4:5] nt
	s_add_u32 s4, s4, s15
	s_addc_u32 s5, s5, 0
	global_load_dword v161, v1, s[4:5] nt
	s_add_u32 s4, s4, s15
	s_addc_u32 s5, s5, 0
	global_load_dword v162, v1, s[4:5] nt
	s_add_u32 s4, s4, s15
	s_addc_u32 s5, s5, 0
	global_load_dword v163, v1, s[4:5] nt
	s_add_u32 s4, s4, s15
	s_addc_u32 s5, s5, 0
	global_load_dword v164, v1, s[4:5] nt
	s_add_u32 s4, s4, s15
	s_addc_u32 s5, s5, 0
	global_load_dword v165, v1, s[4:5] nt
	s_add_u32 s4, s4, s15
	s_addc_u32 s5, s5, 0
	global_load_dword v166, v1, s[4:5] nt
	s_add_u32 s4, s4, s15
	s_addc_u32 s5, s5, 0
	global_load_dword v167, v1, s[4:5] nt
	s_add_u32 s4, s4, s15
	s_addc_u32 s5, s5, 0
	global_load_dword v168, v1, s[4:5] nt
	s_add_u32 s4, s4, s15
	s_addc_u32 s5, s5, 0
	global_load_dword v169, v1, s[4:5] nt
	s_add_u32 s4, s4, s15
	s_addc_u32 s5, s5, 0
	global_load_dword v170, v1, s[4:5] nt
	s_add_u32 s4, s4, s15
	s_addc_u32 s5, s5, 0
	global_load_dword v171, v1, s[4:5] nt
	s_add_u32 s4, s4, s15
	s_addc_u32 s5, s5, 0
	global_load_dword v172, v1, s[4:5] nt
	s_add_u32 s4, s4, s15
	s_addc_u32 s5, s5, 0
	global_load_dword v173, v1, s[4:5] nt
	s_add_u32 s4, s4, s15
	s_addc_u32 s5, s5, 0
	global_load_dword v174, v1, s[4:5] nt
	s_add_u32 s4, s4, s15
	s_addc_u32 s5, s5, 0
	global_load_dword v175, v1, s[4:5] nt
	s_add_u32 s4, s4, s15
	s_addc_u32 s5, s5, 0
	global_load_dword v176, v1, s[4:5] nt
	s_add_u32 s4, s4, s15
	s_addc_u32 s5, s5, 0
	global_load_dword v177, v1, s[4:5] nt
	s_add_u32 s4, s4, s15
	s_addc_u32 s5, s5, 0
	global_load_dword v178, v1, s[4:5] nt
	s_add_u32 s4, s4, s15
	s_addc_u32 s5, s5, 0
	global_load_dword v179, v1, s[4:5] nt
	s_add_u32 s4, s4, s15
	s_addc_u32 s5, s5, 0
	s_waitcnt vmcnt(32)
	v_max3_f32 v206, |v20|, |v21|, |v22|
	v_max3_f32 v206, v206, |v23|, |v24|
	v_max3_f32 v206, v206, |v25|, |v26|
	v_max3_f32 v206, v206, |v27|, |v28|
	v_max3_f32 v206, v206, |v29|, |v30|
	v_max3_f32 v206, v206, |v31|, |v32|
	v_max3_f32 v206, v206, |v33|, |v34|
	v_max3_f32 v206, v206, |v35|, |v36|
	v_max3_f32 v206, v206, |v37|, |v38|
	v_max3_f32 v206, v206, |v39|, |v40|
	v_max3_f32 v206, v206, |v41|, |v42|
	v_max3_f32 v206, v206, |v43|, |v44|
	v_max3_f32 v206, v206, |v45|, |v46|
	v_max3_f32 v206, v206, |v47|, |v48|
	v_max3_f32 v206, v206, |v49|, |v50|
	v_max_f32_e64 v206, v206, |v51|
	v_bfe_u32 v207, v206, 23, 8
	v_and_or_b32 v206, v206, s31, 0.5
	v_cmp_lt_f32_e32 vcc, 0x3f700000, v206
	s_nop 1
	v_addc_co_u32_e32 v207, vcc, 0, v207, vcc
	v_add_u32_e32 v207, 0xffffff7f, v207
	v_max_i32_e32 v207, 0xffffff82, v207
	v_add_u32_e32 v58, 0x7f, v207
	v_lshlrev_b32_e32 v207, 23, v58
	v_mov_b32_e32 v59, 0
	s_nop 0
	v_cvt_scalef32_2xpk16_fp6_f32 v[52:57], v[20:35], v[36:51], v207
	global_load_dword v20, v1, s[4:5] nt
	s_add_u32 s4, s4, s15
	s_addc_u32 s5, s5, 0
	global_load_dword v21, v1, s[4:5] nt
	s_add_u32 s4, s4, s15
	s_addc_u32 s5, s5, 0
	global_load_dword v22, v1, s[4:5] nt
	s_add_u32 s4, s4, s15
	s_addc_u32 s5, s5, 0
	global_load_dword v23, v1, s[4:5] nt
	s_add_u32 s4, s4, s15
	s_addc_u32 s5, s5, 0
	global_load_dword v24, v1, s[4:5] nt
	s_add_u32 s4, s4, s15
	s_addc_u32 s5, s5, 0
	global_load_dword v25, v1, s[4:5] nt
	s_add_u32 s4, s4, s15
	s_addc_u32 s5, s5, 0
	global_load_dword v26, v1, s[4:5] nt
	s_add_u32 s4, s4, s15
	s_addc_u32 s5, s5, 0
	global_load_dword v27, v1, s[4:5] nt
	s_add_u32 s4, s4, s15
	s_addc_u32 s5, s5, 0
	global_load_dword v28, v1, s[4:5] nt
	s_add_u32 s4, s4, s15
	s_addc_u32 s5, s5, 0
	global_load_dword v29, v1, s[4:5] nt
	s_add_u32 s4, s4, s15
	s_addc_u32 s5, s5, 0
	global_load_dword v30, v1, s[4:5] nt
	s_add_u32 s4, s4, s15
	s_addc_u32 s5, s5, 0
	global_load_dword v31, v1, s[4:5] nt
	s_add_u32 s4, s4, s15
	s_addc_u32 s5, s5, 0
	global_load_dword v32, v1, s[4:5] nt
	s_add_u32 s4, s4, s15
	s_addc_u32 s5, s5, 0
	global_load_dword v33, v1, s[4:5] nt
	s_add_u32 s4, s4, s15
	s_addc_u32 s5, s5, 0
	global_load_dword v34, v1, s[4:5] nt
	s_add_u32 s4, s4, s15
	s_addc_u32 s5, s5, 0
	global_load_dword v35, v1, s[4:5] nt
	s_add_u32 s4, s4, s15
	s_addc_u32 s5, s5, 0
	global_load_dword v36, v1, s[4:5] nt
	s_add_u32 s4, s4, s15
	s_addc_u32 s5, s5, 0
	global_load_dword v37, v1, s[4:5] nt
	s_add_u32 s4, s4, s15
	s_addc_u32 s5, s5, 0
	global_load_dword v38, v1, s[4:5] nt
	s_add_u32 s4, s4, s15
	s_addc_u32 s5, s5, 0
	global_load_dword v39, v1, s[4:5] nt
	s_add_u32 s4, s4, s15
	s_addc_u32 s5, s5, 0
	global_load_dword v40, v1, s[4:5] nt
	s_add_u32 s4, s4, s15
	s_addc_u32 s5, s5, 0
	global_load_dword v41, v1, s[4:5] nt
	s_add_u32 s4, s4, s15
	s_addc_u32 s5, s5, 0
	global_load_dword v42, v1, s[4:5] nt
	s_add_u32 s4, s4, s15
	s_addc_u32 s5, s5, 0
	global_load_dword v43, v1, s[4:5] nt
	s_add_u32 s4, s4, s15
	s_addc_u32 s5, s5, 0
	global_load_dword v44, v1, s[4:5] nt
	s_add_u32 s4, s4, s15
	s_addc_u32 s5, s5, 0
	global_load_dword v45, v1, s[4:5] nt
	s_add_u32 s4, s4, s15
	s_addc_u32 s5, s5, 0
	global_load_dword v46, v1, s[4:5] nt
	s_add_u32 s4, s4, s15
	s_addc_u32 s5, s5, 0
	global_load_dword v47, v1, s[4:5] nt
	s_add_u32 s4, s4, s15
	s_addc_u32 s5, s5, 0
	global_load_dword v48, v1, s[4:5] nt
	s_add_u32 s4, s4, s15
	s_addc_u32 s5, s5, 0
	global_load_dword v49, v1, s[4:5] nt
	s_add_u32 s4, s4, s15
	s_addc_u32 s5, s5, 0
	global_load_dword v50, v1, s[4:5] nt
	s_add_u32 s4, s4, s15
	s_addc_u32 s5, s5, 0
	global_load_dword v51, v1, s[4:5] nt
	s_add_u32 s4, s4, s15
	s_addc_u32 s5, s5, 0
	s_waitcnt vmcnt(32)
	v_max3_f32 v206, |v148|, |v149|, |v150|
	v_max3_f32 v206, v206, |v151|, |v152|
	v_max3_f32 v206, v206, |v153|, |v154|
	v_max3_f32 v206, v206, |v155|, |v156|
	v_max3_f32 v206, v206, |v157|, |v158|
	v_max3_f32 v206, v206, |v159|, |v160|
	v_max3_f32 v206, v206, |v161|, |v162|
	v_max3_f32 v206, v206, |v163|, |v164|
	v_max3_f32 v206, v206, |v165|, |v166|
	v_max3_f32 v206, v206, |v167|, |v168|
	v_max3_f32 v206, v206, |v169|, |v170|
	v_max3_f32 v206, v206, |v171|, |v172|
	v_max3_f32 v206, v206, |v173|, |v174|
	v_max3_f32 v206, v206, |v175|, |v176|
	v_max3_f32 v206, v206, |v177|, |v178|
	v_max_f32_e64 v206, v206, |v179|
	v_bfe_u32 v207, v206, 23, 8
	v_and_or_b32 v206, v206, s31, 0.5
	v_cmp_lt_f32_e32 vcc, 0x3f700000, v206
	s_nop 1
	v_addc_co_u32_e32 v207, vcc, 0, v207, vcc
	v_add_u32_e32 v207, 0xffffff7f, v207
	v_max_i32_e32 v207, 0xffffff82, v207
	v_add_u32_e32 v66, 0x7f, v207
	v_lshlrev_b32_e32 v207, 23, v66
	v_mov_b32_e32 v67, 0
	s_nop 0
	v_cvt_scalef32_2xpk16_fp6_f32 v[60:65], v[148:163], v[164:179], v207
	global_load_dword v148, v1, s[4:5] nt
	s_add_u32 s4, s4, s15
	s_addc_u32 s5, s5, 0
	global_load_dword v149, v1, s[4:5] nt
	s_add_u32 s4, s4, s15
	s_addc_u32 s5, s5, 0
	global_load_dword v150, v1, s[4:5] nt
	s_add_u32 s4, s4, s15
	s_addc_u32 s5, s5, 0
	global_load_dword v151, v1, s[4:5] nt
	s_add_u32 s4, s4, s15
	s_addc_u32 s5, s5, 0
	global_load_dword v152, v1, s[4:5] nt
	s_add_u32 s4, s4, s15
	s_addc_u32 s5, s5, 0
	global_load_dword v153, v1, s[4:5] nt
	s_add_u32 s4, s4, s15
	s_addc_u32 s5, s5, 0
	global_load_dword v154, v1, s[4:5] nt
	s_add_u32 s4, s4, s15
	s_addc_u32 s5, s5, 0
	global_load_dword v155, v1, s[4:5] nt
	s_add_u32 s4, s4, s15
	s_addc_u32 s5, s5, 0
	global_load_dword v156, v1, s[4:5] nt
	s_add_u32 s4, s4, s15
	s_addc_u32 s5, s5, 0
	global_load_dword v157, v1, s[4:5] nt
	s_add_u32 s4, s4, s15
	s_addc_u32 s5, s5, 0
	global_load_dword v158, v1, s[4:5] nt
	s_add_u32 s4, s4, s15
	s_addc_u32 s5, s5, 0
	global_load_dword v159, v1, s[4:5] nt
	s_add_u32 s4, s4, s15
	s_addc_u32 s5, s5, 0
	global_load_dword v160, v1, s[4:5] nt
	s_add_u32 s4, s4, s15
	s_addc_u32 s5, s5, 0
	global_load_dword v161, v1, s[4:5] nt
	s_add_u32 s4, s4, s15
	s_addc_u32 s5, s5, 0
	global_load_dword v162, v1, s[4:5] nt
	s_add_u32 s4, s4, s15
	s_addc_u32 s5, s5, 0
	global_load_dword v163, v1, s[4:5] nt
	s_add_u32 s4, s4, s15
	s_addc_u32 s5, s5, 0
	global_load_dword v164, v1, s[4:5] nt
	s_add_u32 s4, s4, s15
	s_addc_u32 s5, s5, 0
	global_load_dword v165, v1, s[4:5] nt
	s_add_u32 s4, s4, s15
	s_addc_u32 s5, s5, 0
	global_load_dword v166, v1, s[4:5] nt
	s_add_u32 s4, s4, s15
	s_addc_u32 s5, s5, 0
	global_load_dword v167, v1, s[4:5] nt
	s_add_u32 s4, s4, s15
	s_addc_u32 s5, s5, 0
	global_load_dword v168, v1, s[4:5] nt
	s_add_u32 s4, s4, s15
	s_addc_u32 s5, s5, 0
	global_load_dword v169, v1, s[4:5] nt
	s_add_u32 s4, s4, s15
	s_addc_u32 s5, s5, 0
	global_load_dword v170, v1, s[4:5] nt
	s_add_u32 s4, s4, s15
	s_addc_u32 s5, s5, 0
	global_load_dword v171, v1, s[4:5] nt
	s_add_u32 s4, s4, s15
	s_addc_u32 s5, s5, 0
	global_load_dword v172, v1, s[4:5] nt
	s_add_u32 s4, s4, s15
	s_addc_u32 s5, s5, 0
	global_load_dword v173, v1, s[4:5] nt
	s_add_u32 s4, s4, s15
	s_addc_u32 s5, s5, 0
	global_load_dword v174, v1, s[4:5] nt
	s_add_u32 s4, s4, s15
	s_addc_u32 s5, s5, 0
	global_load_dword v175, v1, s[4:5] nt
	s_add_u32 s4, s4, s15
	s_addc_u32 s5, s5, 0
	global_load_dword v176, v1, s[4:5] nt
	s_add_u32 s4, s4, s15
	s_addc_u32 s5, s5, 0
	global_load_dword v177, v1, s[4:5] nt
	s_add_u32 s4, s4, s15
	s_addc_u32 s5, s5, 0
	global_load_dword v178, v1, s[4:5] nt
	s_add_u32 s4, s4, s15
	s_addc_u32 s5, s5, 0
	global_load_dword v179, v1, s[4:5] nt
	s_add_u32 s4, s4, s15
	s_addc_u32 s5, s5, 0
	s_waitcnt vmcnt(32)
	v_max3_f32 v206, |v20|, |v21|, |v22|
	v_max3_f32 v206, v206, |v23|, |v24|
	v_max3_f32 v206, v206, |v25|, |v26|
	v_max3_f32 v206, v206, |v27|, |v28|
	v_max3_f32 v206, v206, |v29|, |v30|
	v_max3_f32 v206, v206, |v31|, |v32|
	v_max3_f32 v206, v206, |v33|, |v34|
	v_max3_f32 v206, v206, |v35|, |v36|
	v_max3_f32 v206, v206, |v37|, |v38|
	v_max3_f32 v206, v206, |v39|, |v40|
	v_max3_f32 v206, v206, |v41|, |v42|
	v_max3_f32 v206, v206, |v43|, |v44|
	v_max3_f32 v206, v206, |v45|, |v46|
	v_max3_f32 v206, v206, |v47|, |v48|
	v_max3_f32 v206, v206, |v49|, |v50|
	v_max_f32_e64 v206, v206, |v51|
	v_bfe_u32 v207, v206, 23, 8
	v_and_or_b32 v206, v206, s31, 0.5
	v_cmp_lt_f32_e32 vcc, 0x3f700000, v206
	s_nop 1
	v_addc_co_u32_e32 v207, vcc, 0, v207, vcc
	v_add_u32_e32 v207, 0xffffff7f, v207
	v_max_i32_e32 v207, 0xffffff82, v207
	v_add_u32_e32 v226, 0x7f, v207
	v_lshlrev_b32_e32 v207, 23, v226
	v_mov_b32_e32 v227, 0
	s_nop 0
	v_cvt_scalef32_2xpk16_fp6_f32 v[220:225], v[20:35], v[36:51], v207
	s_waitcnt vmcnt(0)
	v_max3_f32 v206, |v148|, |v149|, |v150|
	v_max3_f32 v206, v206, |v151|, |v152|
	v_max3_f32 v206, v206, |v153|, |v154|
	v_max3_f32 v206, v206, |v155|, |v156|
	v_max3_f32 v206, v206, |v157|, |v158|
	v_max3_f32 v206, v206, |v159|, |v160|
	v_max3_f32 v206, v206, |v161|, |v162|
	v_max3_f32 v206, v206, |v163|, |v164|
	v_max3_f32 v206, v206, |v165|, |v166|
	v_max3_f32 v206, v206, |v167|, |v168|
	v_max3_f32 v206, v206, |v169|, |v170|
	v_max3_f32 v206, v206, |v171|, |v172|
	v_max3_f32 v206, v206, |v173|, |v174|
	v_max3_f32 v206, v206, |v175|, |v176|
	v_max3_f32 v206, v206, |v177|, |v178|
	v_max_f32_e64 v206, v206, |v179|
	v_bfe_u32 v207, v206, 23, 8
	v_and_or_b32 v206, v206, s31, 0.5
	v_cmp_lt_f32_e32 vcc, 0x3f700000, v206
	s_nop 1
	v_addc_co_u32_e32 v207, vcc, 0, v207, vcc
	v_add_u32_e32 v207, 0xffffff7f, v207
	v_max_i32_e32 v207, 0xffffff82, v207
	v_add_u32_e32 v234, 0x7f, v207
	v_lshlrev_b32_e32 v207, 23, v234
	v_mov_b32_e32 v235, 0
	s_nop 0
	v_cvt_scalef32_2xpk16_fp6_f32 v[228:233], v[148:163], v[164:179], v207
	s_nop 4
	global_store_dwordx4 v2, v[52:55], s[8:9]
	global_store_dwordx4 v2, v[60:63], s[8:9] offset:16
	global_store_dwordx4 v2, v[220:223], s[8:9] offset:32
	global_store_dwordx4 v2, v[228:231], s[8:9] offset:48
	global_store_dwordx4 v2, v[56:59], s[8:9] offset:64
	global_store_dwordx4 v2, v[64:67], s[8:9] offset:80
	global_store_dwordx4 v2, v[224:227], s[8:9] offset:96
	global_store_dwordx4 v2, v[232:235], s[8:9] offset:112
	s_branch .Lcv_next
.Lcv_fp8:
	s_sub_i32 s3, s0, 14
	s_lshl_b32 s3, s3, 11
	s_add_i32 s3, s3, s47
	s_lshr_b32 s16, s3, 8
	s_mul_i32 s16, s16, 37
	s_lshr_b32 s16, s16, 8
	s_mul_i32 s44, s16, 0x700
	s_sub_i32 s3, s3, s44
	s_lshr_b32 s44, s3, 5
	s_and_b32 s3, s3, 31
	s_load_dwordx2 s[6:7], s[40:41], 0x118
	s_mul_i32 s12, s16, 0x3800000
	s_lshl_b32 s13, s44, 20
	s_add_u32 s12, s12, s13
	s_lshl_b32 s13, s3, 8
	s_add_u32 s12, s12, s13
	s_mov_b32 s15, 0x2000
	s_waitcnt lgkmcnt(0)
	s_add_u32 s4, s6, s12
	s_addc_u32 s5, s7, 0
	s_mul_i32 s12, s16, 0xe00000
	s_lshl_b32 s13, s44, 7
	s_add_u32 s12, s12, s13
	s_add_u32 s12, s12, 0x24400000
	s_add_u32 s8, s34, s12
	s_addc_u32 s9, s35, 0
	v_lshl_add_u32 v5, s3, 6, v0
	v_mul_u32_u24_e32 v2, 0x1c00, v5
	global_load_dword v20, v1, s[4:5] nt
	s_add_u32 s4, s4, s15
	s_addc_u32 s5, s5, 0
	global_load_dword v21, v1, s[4:5] nt
	s_add_u32 s4, s4, s15
	s_addc_u32 s5, s5, 0
	global_load_dword v22, v1, s[4:5] nt
	s_add_u32 s4, s4, s15
	s_addc_u32 s5, s5, 0
	global_load_dword v23, v1, s[4:5] nt
	s_add_u32 s4, s4, s15
	s_addc_u32 s5, s5, 0
	global_load_dword v24, v1, s[4:5] nt
	s_add_u32 s4, s4, s15
	s_addc_u32 s5, s5, 0
	global_load_dword v25, v1, s[4:5] nt
	s_add_u32 s4, s4, s15
	s_addc_u32 s5, s5, 0
	global_load_dword v26, v1, s[4:5] nt
	s_add_u32 s4, s4, s15
	s_addc_u32 s5, s5, 0
	global_load_dword v27, v1, s[4:5] nt
	s_add_u32 s4, s4, s15
	s_addc_u32 s5, s5, 0
	global_load_dword v28, v1, s[4:5] nt
	s_add_u32 s4, s4, s15
	s_addc_u32 s5, s5, 0
	global_load_dword v29, v1, s[4:5] nt
	s_add_u32 s4, s4, s15
	s_addc_u32 s5, s5, 0
	global_load_dword v30, v1, s[4:5] nt
	s_add_u32 s4, s4, s15
	s_addc_u32 s5, s5, 0
	global_load_dword v31, v1, s[4:5] nt
	s_add_u32 s4, s4, s15
	s_addc_u32 s5, s5, 0
	global_load_dword v32, v1, s[4:5] nt
	s_add_u32 s4, s4, s15
	s_addc_u32 s5, s5, 0
	global_load_dword v33, v1, s[4:5] nt
	s_add_u32 s4, s4, s15
	s_addc_u32 s5, s5, 0
	global_load_dword v34, v1, s[4:5] nt
	s_add_u32 s4, s4, s15
	s_addc_u32 s5, s5, 0
	global_load_dword v35, v1, s[4:5] nt
	s_add_u32 s4, s4, s15
	s_addc_u32 s5, s5, 0
	global_load_dword v36, v1, s[4:5] nt
	s_add_u32 s4, s4, s15
	s_addc_u32 s5, s5, 0
	global_load_dword v37, v1, s[4:5] nt
	s_add_u32 s4, s4, s15
	s_addc_u32 s5, s5, 0
	global_load_dword v38, v1, s[4:5] nt
	s_add_u32 s4, s4, s15
	s_addc_u32 s5, s5, 0
	global_load_dword v39, v1, s[4:5] nt
	s_add_u32 s4, s4, s15
	s_addc_u32 s5, s5, 0
	global_load_dword v40, v1, s[4:5] nt
	s_add_u32 s4, s4, s15
	s_addc_u32 s5, s5, 0
	global_load_dword v41, v1, s[4:5] nt
	s_add_u32 s4, s4, s15
	s_addc_u32 s5, s5, 0
	global_load_dword v42, v1, s[4:5] nt
	s_add_u32 s4, s4, s15
	s_addc_u32 s5, s5, 0
	global_load_dword v43, v1, s[4:5] nt
	s_add_u32 s4, s4, s15
	s_addc_u32 s5, s5, 0
	global_load_dword v44, v1, s[4:5] nt
	s_add_u32 s4, s4, s15
	s_addc_u32 s5, s5, 0
	global_load_dword v45, v1, s[4:5] nt
	s_add_u32 s4, s4, s15
	s_addc_u32 s5, s5, 0
	global_load_dword v46, v1, s[4:5] nt
	s_add_u32 s4, s4, s15
	s_addc_u32 s5, s5, 0
	global_load_dword v47, v1, s[4:5] nt
	s_add_u32 s4, s4, s15
	s_addc_u32 s5, s5, 0
	global_load_dword v48, v1, s[4:5] nt
	s_add_u32 s4, s4, s15
	s_addc_u32 s5, s5, 0
	global_load_dword v49, v1, s[4:5] nt
	s_add_u32 s4, s4, s15
	s_addc_u32 s5, s5, 0
	global_load_dword v50, v1, s[4:5] nt
	s_add_u32 s4, s4, s15
	s_addc_u32 s5, s5, 0
	global_load_dword v51, v1, s[4:5] nt
	s_add_u32 s4, s4, s15
	s_addc_u32 s5, s5, 0
	global_load_dword v148, v1, s[4:5] nt
	s_add_u32 s4, s4, s15
	s_addc_u32 s5, s5, 0
	global_load_dword v149, v1, s[4:5] nt
	s_add_u32 s4, s4, s15
	s_addc_u32 s5, s5, 0
	global_load_dword v150, v1, s[4:5] nt
	s_add_u32 s4, s4, s15
	s_addc_u32 s5, s5, 0
	global_load_dword v151, v1, s[4:5] nt
	s_add_u32 s4, s4, s15
	s_addc_u32 s5, s5, 0
	global_load_dword v152, v1, s[4:5] nt
	s_add_u32 s4, s4, s15
	s_addc_u32 s5, s5, 0
	global_load_dword v153, v1, s[4:5] nt
	s_add_u32 s4, s4, s15
	s_addc_u32 s5, s5, 0
	global_load_dword v154, v1, s[4:5] nt
	s_add_u32 s4, s4, s15
	s_addc_u32 s5, s5, 0
	global_load_dword v155, v1, s[4:5] nt
	s_add_u32 s4, s4, s15
	s_addc_u32 s5, s5, 0
	global_load_dword v156, v1, s[4:5] nt
	s_add_u32 s4, s4, s15
	s_addc_u32 s5, s5, 0
	global_load_dword v157, v1, s[4:5] nt
	s_add_u32 s4, s4, s15
	s_addc_u32 s5, s5, 0
	global_load_dword v158, v1, s[4:5] nt
	s_add_u32 s4, s4, s15
	s_addc_u32 s5, s5, 0
	global_load_dword v159, v1, s[4:5] nt
	s_add_u32 s4, s4, s15
	s_addc_u32 s5, s5, 0
	global_load_dword v160, v1, s[4:5] nt
	s_add_u32 s4, s4, s15
	s_addc_u32 s5, s5, 0
	global_load_dword v161, v1, s[4:5] nt
	s_add_u32 s4, s4, s15
	s_addc_u32 s5, s5, 0
	global_load_dword v162, v1, s[4:5] nt
	s_add_u32 s4, s4, s15
	s_addc_u32 s5, s5, 0
	global_load_dword v163, v1, s[4:5] nt
	s_add_u32 s4, s4, s15
	s_addc_u32 s5, s5, 0
	global_load_dword v164, v1, s[4:5] nt
	s_add_u32 s4, s4, s15
	s_addc_u32 s5, s5, 0
	global_load_dword v165, v1, s[4:5] nt
	s_add_u32 s4, s4, s15
	s_addc_u32 s5, s5, 0
	global_load_dword v166, v1, s[4:5] nt
	s_add_u32 s4, s4, s15
	s_addc_u32 s5, s5, 0
	global_load_dword v167, v1, s[4:5] nt
	s_add_u32 s4, s4, s15
	s_addc_u32 s5, s5, 0
	global_load_dword v168, v1, s[4:5] nt
	s_add_u32 s4, s4, s15
	s_addc_u32 s5, s5, 0
	global_load_dword v169, v1, s[4:5] nt
	s_add_u32 s4, s4, s15
	s_addc_u32 s5, s5, 0
	global_load_dword v170, v1, s[4:5] nt
	s_add_u32 s4, s4, s15
	s_addc_u32 s5, s5, 0
	global_load_dword v171, v1, s[4:5] nt
	s_add_u32 s4, s4, s15
	s_addc_u32 s5, s5, 0
	global_load_dword v172, v1, s[4:5] nt
	s_add_u32 s4, s4, s15
	s_addc_u32 s5, s5, 0
	global_load_dword v173, v1, s[4:5] nt
	s_add_u32 s4, s4, s15
	s_addc_u32 s5, s5, 0
	global_load_dword v174, v1, s[4:5] nt
	s_add_u32 s4, s4, s15
	s_addc_u32 s5, s5, 0
	global_load_dword v175, v1, s[4:5] nt
	s_add_u32 s4, s4, s15
	s_addc_u32 s5, s5, 0
	global_load_dword v176, v1, s[4:5] nt
	s_add_u32 s4, s4, s15
	s_addc_u32 s5, s5, 0
	global_load_dword v177, v1, s[4:5] nt
	s_add_u32 s4, s4, s15
	s_addc_u32 s5, s5, 0
	global_load_dword v178, v1, s[4:5] nt
	s_add_u32 s4, s4, s15
	s_addc_u32 s5, s5, 0
	global_load_dword v179, v1, s[4:5] nt
	s_add_u32 s4, s4, s15
	s_addc_u32 s5, s5, 0
	s_waitcnt vmcnt(32)
	v_mul_f32_e32 v20, 0x42800000, v20
	v_mul_f32_e32 v21, 0x42800000, v21
	v_mul_f32_e32 v22, 0x42800000, v22
	v_mul_f32_e32 v23, 0x42800000, v23
	v_mul_f32_e32 v24, 0x42800000, v24
	v_mul_f32_e32 v25, 0x42800000, v25
	v_mul_f32_e32 v26, 0x42800000, v26
	v_mul_f32_e32 v27, 0x42800000, v27
	v_mul_f32_e32 v28, 0x42800000, v28
	v_mul_f32_e32 v29, 0x42800000, v29
	v_mul_f32_e32 v30, 0x42800000, v30
	v_mul_f32_e32 v31, 0x42800000, v31
	v_mul_f32_e32 v32, 0x42800000, v32
	v_mul_f32_e32 v33, 0x42800000, v33
	v_mul_f32_e32 v34, 0x42800000, v34
	v_mul_f32_e32 v35, 0x42800000, v35
	v_mul_f32_e32 v36, 0x42800000, v36
	v_mul_f32_e32 v37, 0x42800000, v37
	v_mul_f32_e32 v38, 0x42800000, v38
	v_mul_f32_e32 v39, 0x42800000, v39
	v_mul_f32_e32 v40, 0x42800000, v40
	v_mul_f32_e32 v41, 0x42800000, v41
	v_mul_f32_e32 v42, 0x42800000, v42
	v_mul_f32_e32 v43, 0x42800000, v43
	v_mul_f32_e32 v44, 0x42800000, v44
	v_mul_f32_e32 v45, 0x42800000, v45
	v_mul_f32_e32 v46, 0x42800000, v46
	v_mul_f32_e32 v47, 0x42800000, v47
	v_mul_f32_e32 v48, 0x42800000, v48
	v_mul_f32_e32 v49, 0x42800000, v49
	v_mul_f32_e32 v50, 0x42800000, v50
	v_mul_f32_e32 v51, 0x42800000, v51
	v_cvt_pk_fp8_f32 v52, v20, v21
	v_cvt_pk_fp8_f32 v52, v22, v23 op_sel:[0,0,1]
	v_cvt_pk_fp8_f32 v53, v24, v25
	v_cvt_pk_fp8_f32 v53, v26, v27 op_sel:[0,0,1]
	v_cvt_pk_fp8_f32 v54, v28, v29
	v_cvt_pk_fp8_f32 v54, v30, v31 op_sel:[0,0,1]
	v_cvt_pk_fp8_f32 v55, v32, v33
	v_cvt_pk_fp8_f32 v55, v34, v35 op_sel:[0,0,1]
	v_cvt_pk_fp8_f32 v56, v36, v37
	v_cvt_pk_fp8_f32 v56, v38, v39 op_sel:[0,0,1]
	v_cvt_pk_fp8_f32 v57, v40, v41
	v_cvt_pk_fp8_f32 v57, v42, v43 op_sel:[0,0,1]
	v_cvt_pk_fp8_f32 v58, v44, v45
	v_cvt_pk_fp8_f32 v58, v46, v47 op_sel:[0,0,1]
	v_cvt_pk_fp8_f32 v59, v48, v49
	v_cvt_pk_fp8_f32 v59, v50, v51 op_sel:[0,0,1]
	global_load_dword v20, v1, s[4:5] nt
	s_add_u32 s4, s4, s15
	s_addc_u32 s5, s5, 0
	global_load_dword v21, v1, s[4:5] nt
	s_add_u32 s4, s4, s15
	s_addc_u32 s5, s5, 0
	global_load_dword v22, v1, s[4:5] nt
	s_add_u32 s4, s4, s15
	s_addc_u32 s5, s5, 0
	global_load_dword v23, v1, s[4:5] nt
	s_add_u32 s4, s4, s15
	s_addc_u32 s5, s5, 0
	global_load_dword v24, v1, s[4:5] nt
	s_add_u32 s4, s4, s15
	s_addc_u32 s5, s5, 0
	global_load_dword v25, v1, s[4:5] nt
	s_add_u32 s4, s4, s15
	s_addc_u32 s5, s5, 0
	global_load_dword v26, v1, s[4:5] nt
	s_add_u32 s4, s4, s15
	s_addc_u32 s5, s5, 0
	global_load_dword v27, v1, s[4:5] nt
	s_add_u32 s4, s4, s15
	s_addc_u32 s5, s5, 0
	global_load_dword v28, v1, s[4:5] nt
	s_add_u32 s4, s4, s15
	s_addc_u32 s5, s5, 0
	global_load_dword v29, v1, s[4:5] nt
	s_add_u32 s4, s4, s15
	s_addc_u32 s5, s5, 0
	global_load_dword v30, v1, s[4:5] nt
	s_add_u32 s4, s4, s15
	s_addc_u32 s5, s5, 0
	global_load_dword v31, v1, s[4:5] nt
	s_add_u32 s4, s4, s15
	s_addc_u32 s5, s5, 0
	global_load_dword v32, v1, s[4:5] nt
	s_add_u32 s4, s4, s15
	s_addc_u32 s5, s5, 0
	global_load_dword v33, v1, s[4:5] nt
	s_add_u32 s4, s4, s15
	s_addc_u32 s5, s5, 0
	global_load_dword v34, v1, s[4:5] nt
	s_add_u32 s4, s4, s15
	s_addc_u32 s5, s5, 0
	global_load_dword v35, v1, s[4:5] nt
	s_add_u32 s4, s4, s15
	s_addc_u32 s5, s5, 0
	global_load_dword v36, v1, s[4:5] nt
	s_add_u32 s4, s4, s15
	s_addc_u32 s5, s5, 0
	global_load_dword v37, v1, s[4:5] nt
	s_add_u32 s4, s4, s15
	s_addc_u32 s5, s5, 0
	global_load_dword v38, v1, s[4:5] nt
	s_add_u32 s4, s4, s15
	s_addc_u32 s5, s5, 0
	global_load_dword v39, v1, s[4:5] nt
	s_add_u32 s4, s4, s15
	s_addc_u32 s5, s5, 0
	global_load_dword v40, v1, s[4:5] nt
	s_add_u32 s4, s4, s15
	s_addc_u32 s5, s5, 0
	global_load_dword v41, v1, s[4:5] nt
	s_add_u32 s4, s4, s15
	s_addc_u32 s5, s5, 0
	global_load_dword v42, v1, s[4:5] nt
	s_add_u32 s4, s4, s15
	s_addc_u32 s5, s5, 0
	global_load_dword v43, v1, s[4:5] nt
	s_add_u32 s4, s4, s15
	s_addc_u32 s5, s5, 0
	global_load_dword v44, v1, s[4:5] nt
	s_add_u32 s4, s4, s15
	s_addc_u32 s5, s5, 0
	global_load_dword v45, v1, s[4:5] nt
	s_add_u32 s4, s4, s15
	s_addc_u32 s5, s5, 0
	global_load_dword v46, v1, s[4:5] nt
	s_add_u32 s4, s4, s15
	s_addc_u32 s5, s5, 0
	global_load_dword v47, v1, s[4:5] nt
	s_add_u32 s4, s4, s15
	s_addc_u32 s5, s5, 0
	global_load_dword v48, v1, s[4:5] nt
	s_add_u32 s4, s4, s15
	s_addc_u32 s5, s5, 0
	global_load_dword v49, v1, s[4:5] nt
	s_add_u32 s4, s4, s15
	s_addc_u32 s5, s5, 0
	global_load_dword v50, v1, s[4:5] nt
	s_add_u32 s4, s4, s15
	s_addc_u32 s5, s5, 0
	global_load_dword v51, v1, s[4:5] nt
	s_add_u32 s4, s4, s15
	s_addc_u32 s5, s5, 0
	s_waitcnt vmcnt(32)
	v_mul_f32_e32 v148, 0x42800000, v148
	v_mul_f32_e32 v149, 0x42800000, v149
	v_mul_f32_e32 v150, 0x42800000, v150
	v_mul_f32_e32 v151, 0x42800000, v151
	v_mul_f32_e32 v152, 0x42800000, v152
	v_mul_f32_e32 v153, 0x42800000, v153
	v_mul_f32_e32 v154, 0x42800000, v154
	v_mul_f32_e32 v155, 0x42800000, v155
	v_mul_f32_e32 v156, 0x42800000, v156
	v_mul_f32_e32 v157, 0x42800000, v157
	v_mul_f32_e32 v158, 0x42800000, v158
	v_mul_f32_e32 v159, 0x42800000, v159
	v_mul_f32_e32 v160, 0x42800000, v160
	v_mul_f32_e32 v161, 0x42800000, v161
	v_mul_f32_e32 v162, 0x42800000, v162
	v_mul_f32_e32 v163, 0x42800000, v163
	v_mul_f32_e32 v164, 0x42800000, v164
	v_mul_f32_e32 v165, 0x42800000, v165
	v_mul_f32_e32 v166, 0x42800000, v166
	v_mul_f32_e32 v167, 0x42800000, v167
	v_mul_f32_e32 v168, 0x42800000, v168
	v_mul_f32_e32 v169, 0x42800000, v169
	v_mul_f32_e32 v170, 0x42800000, v170
	v_mul_f32_e32 v171, 0x42800000, v171
	v_mul_f32_e32 v172, 0x42800000, v172
	v_mul_f32_e32 v173, 0x42800000, v173
	v_mul_f32_e32 v174, 0x42800000, v174
	v_mul_f32_e32 v175, 0x42800000, v175
	v_mul_f32_e32 v176, 0x42800000, v176
	v_mul_f32_e32 v177, 0x42800000, v177
	v_mul_f32_e32 v178, 0x42800000, v178
	v_mul_f32_e32 v179, 0x42800000, v179
	v_cvt_pk_fp8_f32 v60, v148, v149
	v_cvt_pk_fp8_f32 v60, v150, v151 op_sel:[0,0,1]
	v_cvt_pk_fp8_f32 v61, v152, v153
	v_cvt_pk_fp8_f32 v61, v154, v155 op_sel:[0,0,1]
	v_cvt_pk_fp8_f32 v62, v156, v157
	v_cvt_pk_fp8_f32 v62, v158, v159 op_sel:[0,0,1]
	v_cvt_pk_fp8_f32 v63, v160, v161
	v_cvt_pk_fp8_f32 v63, v162, v163 op_sel:[0,0,1]
	v_cvt_pk_fp8_f32 v64, v164, v165
	v_cvt_pk_fp8_f32 v64, v166, v167 op_sel:[0,0,1]
	v_cvt_pk_fp8_f32 v65, v168, v169
	v_cvt_pk_fp8_f32 v65, v170, v171 op_sel:[0,0,1]
	v_cvt_pk_fp8_f32 v66, v172, v173
	v_cvt_pk_fp8_f32 v66, v174, v175 op_sel:[0,0,1]
	v_cvt_pk_fp8_f32 v67, v176, v177
	v_cvt_pk_fp8_f32 v67, v178, v179 op_sel:[0,0,1]
	global_load_dword v148, v1, s[4:5] nt
	s_add_u32 s4, s4, s15
	s_addc_u32 s5, s5, 0
	global_load_dword v149, v1, s[4:5] nt
	s_add_u32 s4, s4, s15
	s_addc_u32 s5, s5, 0
	global_load_dword v150, v1, s[4:5] nt
	s_add_u32 s4, s4, s15
	s_addc_u32 s5, s5, 0
	global_load_dword v151, v1, s[4:5] nt
	s_add_u32 s4, s4, s15
	s_addc_u32 s5, s5, 0
	global_load_dword v152, v1, s[4:5] nt
	s_add_u32 s4, s4, s15
	s_addc_u32 s5, s5, 0
	global_load_dword v153, v1, s[4:5] nt
	s_add_u32 s4, s4, s15
	s_addc_u32 s5, s5, 0
	global_load_dword v154, v1, s[4:5] nt
	s_add_u32 s4, s4, s15
	s_addc_u32 s5, s5, 0
	global_load_dword v155, v1, s[4:5] nt
	s_add_u32 s4, s4, s15
	s_addc_u32 s5, s5, 0
	global_load_dword v156, v1, s[4:5] nt
	s_add_u32 s4, s4, s15
	s_addc_u32 s5, s5, 0
	global_load_dword v157, v1, s[4:5] nt
	s_add_u32 s4, s4, s15
	s_addc_u32 s5, s5, 0
	global_load_dword v158, v1, s[4:5] nt
	s_add_u32 s4, s4, s15
	s_addc_u32 s5, s5, 0
	global_load_dword v159, v1, s[4:5] nt
	s_add_u32 s4, s4, s15
	s_addc_u32 s5, s5, 0
	global_load_dword v160, v1, s[4:5] nt
	s_add_u32 s4, s4, s15
	s_addc_u32 s5, s5, 0
	global_load_dword v161, v1, s[4:5] nt
	s_add_u32 s4, s4, s15
	s_addc_u32 s5, s5, 0
	global_load_dword v162, v1, s[4:5] nt
	s_add_u32 s4, s4, s15
	s_addc_u32 s5, s5, 0
	global_load_dword v163, v1, s[4:5] nt
	s_add_u32 s4, s4, s15
	s_addc_u32 s5, s5, 0
	global_load_dword v164, v1, s[4:5] nt
	s_add_u32 s4, s4, s15
	s_addc_u32 s5, s5, 0
	global_load_dword v165, v1, s[4:5] nt
	s_add_u32 s4, s4, s15
	s_addc_u32 s5, s5, 0
	global_load_dword v166, v1, s[4:5] nt
	s_add_u32 s4, s4, s15
	s_addc_u32 s5, s5, 0
	global_load_dword v167, v1, s[4:5] nt
	s_add_u32 s4, s4, s15
	s_addc_u32 s5, s5, 0
	global_load_dword v168, v1, s[4:5] nt
	s_add_u32 s4, s4, s15
	s_addc_u32 s5, s5, 0
	global_load_dword v169, v1, s[4:5] nt
	s_add_u32 s4, s4, s15
	s_addc_u32 s5, s5, 0
	global_load_dword v170, v1, s[4:5] nt
	s_add_u32 s4, s4, s15
	s_addc_u32 s5, s5, 0
	global_load_dword v171, v1, s[4:5] nt
	s_add_u32 s4, s4, s15
	s_addc_u32 s5, s5, 0
	global_load_dword v172, v1, s[4:5] nt
	s_add_u32 s4, s4, s15
	s_addc_u32 s5, s5, 0
	global_load_dword v173, v1, s[4:5] nt
	s_add_u32 s4, s4, s15
	s_addc_u32 s5, s5, 0
	global_load_dword v174, v1, s[4:5] nt
	s_add_u32 s4, s4, s15
	s_addc_u32 s5, s5, 0
	global_load_dword v175, v1, s[4:5] nt
	s_add_u32 s4, s4, s15
	s_addc_u32 s5, s5, 0
	global_load_dword v176, v1, s[4:5] nt
	s_add_u32 s4, s4, s15
	s_addc_u32 s5, s5, 0
	global_load_dword v177, v1, s[4:5] nt
	s_add_u32 s4, s4, s15
	s_addc_u32 s5, s5, 0
	global_load_dword v178, v1, s[4:5] nt
	s_add_u32 s4, s4, s15
	s_addc_u32 s5, s5, 0
	global_load_dword v179, v1, s[4:5] nt
	s_add_u32 s4, s4, s15
	s_addc_u32 s5, s5, 0
	s_waitcnt vmcnt(32)
	v_mul_f32_e32 v20, 0x42800000, v20
	v_mul_f32_e32 v21, 0x42800000, v21
	v_mul_f32_e32 v22, 0x42800000, v22
	v_mul_f32_e32 v23, 0x42800000, v23
	v_mul_f32_e32 v24, 0x42800000, v24
	v_mul_f32_e32 v25, 0x42800000, v25
	v_mul_f32_e32 v26, 0x42800000, v26
	v_mul_f32_e32 v27, 0x42800000, v27
	v_mul_f32_e32 v28, 0x42800000, v28
	v_mul_f32_e32 v29, 0x42800000, v29
	v_mul_f32_e32 v30, 0x42800000, v30
	v_mul_f32_e32 v31, 0x42800000, v31
	v_mul_f32_e32 v32, 0x42800000, v32
	v_mul_f32_e32 v33, 0x42800000, v33
	v_mul_f32_e32 v34, 0x42800000, v34
	v_mul_f32_e32 v35, 0x42800000, v35
	v_mul_f32_e32 v36, 0x42800000, v36
	v_mul_f32_e32 v37, 0x42800000, v37
	v_mul_f32_e32 v38, 0x42800000, v38
	v_mul_f32_e32 v39, 0x42800000, v39
	v_mul_f32_e32 v40, 0x42800000, v40
	v_mul_f32_e32 v41, 0x42800000, v41
	v_mul_f32_e32 v42, 0x42800000, v42
	v_mul_f32_e32 v43, 0x42800000, v43
	v_mul_f32_e32 v44, 0x42800000, v44
	v_mul_f32_e32 v45, 0x42800000, v45
	v_mul_f32_e32 v46, 0x42800000, v46
	v_mul_f32_e32 v47, 0x42800000, v47
	v_mul_f32_e32 v48, 0x42800000, v48
	v_mul_f32_e32 v49, 0x42800000, v49
	v_mul_f32_e32 v50, 0x42800000, v50
	v_mul_f32_e32 v51, 0x42800000, v51
	v_cvt_pk_fp8_f32 v220, v20, v21
	v_cvt_pk_fp8_f32 v220, v22, v23 op_sel:[0,0,1]
	v_cvt_pk_fp8_f32 v221, v24, v25
	v_cvt_pk_fp8_f32 v221, v26, v27 op_sel:[0,0,1]
	v_cvt_pk_fp8_f32 v222, v28, v29
	v_cvt_pk_fp8_f32 v222, v30, v31 op_sel:[0,0,1]
	v_cvt_pk_fp8_f32 v223, v32, v33
	v_cvt_pk_fp8_f32 v223, v34, v35 op_sel:[0,0,1]
	v_cvt_pk_fp8_f32 v224, v36, v37
	v_cvt_pk_fp8_f32 v224, v38, v39 op_sel:[0,0,1]
	v_cvt_pk_fp8_f32 v225, v40, v41
	v_cvt_pk_fp8_f32 v225, v42, v43 op_sel:[0,0,1]
	v_cvt_pk_fp8_f32 v226, v44, v45
	v_cvt_pk_fp8_f32 v226, v46, v47 op_sel:[0,0,1]
	v_cvt_pk_fp8_f32 v227, v48, v49
	v_cvt_pk_fp8_f32 v227, v50, v51 op_sel:[0,0,1]
	s_waitcnt vmcnt(0)
	v_mul_f32_e32 v148, 0x42800000, v148
	v_mul_f32_e32 v149, 0x42800000, v149
	v_mul_f32_e32 v150, 0x42800000, v150
	v_mul_f32_e32 v151, 0x42800000, v151
	v_mul_f32_e32 v152, 0x42800000, v152
	v_mul_f32_e32 v153, 0x42800000, v153
	v_mul_f32_e32 v154, 0x42800000, v154
	v_mul_f32_e32 v155, 0x42800000, v155
	v_mul_f32_e32 v156, 0x42800000, v156
	v_mul_f32_e32 v157, 0x42800000, v157
	v_mul_f32_e32 v158, 0x42800000, v158
	v_mul_f32_e32 v159, 0x42800000, v159
	v_mul_f32_e32 v160, 0x42800000, v160
	v_mul_f32_e32 v161, 0x42800000, v161
	v_mul_f32_e32 v162, 0x42800000, v162
	v_mul_f32_e32 v163, 0x42800000, v163
	v_mul_f32_e32 v164, 0x42800000, v164
	v_mul_f32_e32 v165, 0x42800000, v165
	v_mul_f32_e32 v166, 0x42800000, v166
	v_mul_f32_e32 v167, 0x42800000, v167
	v_mul_f32_e32 v168, 0x42800000, v168
	v_mul_f32_e32 v169, 0x42800000, v169
	v_mul_f32_e32 v170, 0x42800000, v170
	v_mul_f32_e32 v171, 0x42800000, v171
	v_mul_f32_e32 v172, 0x42800000, v172
	v_mul_f32_e32 v173, 0x42800000, v173
	v_mul_f32_e32 v174, 0x42800000, v174
	v_mul_f32_e32 v175, 0x42800000, v175
	v_mul_f32_e32 v176, 0x42800000, v176
	v_mul_f32_e32 v177, 0x42800000, v177
	v_mul_f32_e32 v178, 0x42800000, v178
	v_mul_f32_e32 v179, 0x42800000, v179
	v_cvt_pk_fp8_f32 v228, v148, v149
	v_cvt_pk_fp8_f32 v228, v150, v151 op_sel:[0,0,1]
	v_cvt_pk_fp8_f32 v229, v152, v153
	v_cvt_pk_fp8_f32 v229, v154, v155 op_sel:[0,0,1]
	v_cvt_pk_fp8_f32 v230, v156, v157
	v_cvt_pk_fp8_f32 v230, v158, v159 op_sel:[0,0,1]
	v_cvt_pk_fp8_f32 v231, v160, v161
	v_cvt_pk_fp8_f32 v231, v162, v163 op_sel:[0,0,1]
	v_cvt_pk_fp8_f32 v232, v164, v165
	v_cvt_pk_fp8_f32 v232, v166, v167 op_sel:[0,0,1]
	v_cvt_pk_fp8_f32 v233, v168, v169
	v_cvt_pk_fp8_f32 v233, v170, v171 op_sel:[0,0,1]
	v_cvt_pk_fp8_f32 v234, v172, v173
	v_cvt_pk_fp8_f32 v234, v174, v175 op_sel:[0,0,1]
	v_cvt_pk_fp8_f32 v235, v176, v177
	v_cvt_pk_fp8_f32 v235, v178, v179 op_sel:[0,0,1]
	s_nop 4
	global_store_dwordx4 v2, v[52:55], s[8:9]
	global_store_dwordx4 v2, v[56:59], s[8:9] offset:16
	global_store_dwordx4 v2, v[60:63], s[8:9] offset:32
	global_store_dwordx4 v2, v[64:67], s[8:9] offset:48
	global_store_dwordx4 v2, v[220:223], s[8:9] offset:64
	global_store_dwordx4 v2, v[224:227], s[8:9] offset:80
	global_store_dwordx4 v2, v[228:231], s[8:9] offset:96
	global_store_dwordx4 v2, v[232:235], s[8:9] offset:112
.Lcv_next:
	s_add_i32 s0, s0, 1
	s_cmp_lt_u32 s0, 21
	s_cbranch_scc1 .Lcv_unit
	s_waitcnt vmcnt(0) lgkmcnt(0)
	s_cmp_eq_u32 s53, 0
	s_cbranch_scc1 .Lcv_ret0
	s_branch .Lcv_ret1
